# edge1: XCD-aware tile assignment (each XCD takes runs of 16 consecutive workgroups' tiles so its L2 serves gathers from few graphs)
# speedup vs baseline: 1.0242x; 1.0058x over previous
.LBB4_4:
	s_or_b64 exec, exec, s[6:7]
	s_and_b32 s86, s2, 7
	s_lshl_b32 s86, s86, 4
	s_bfe_u32 s87, s2, 0x40003
	s_or_b32 s86, s86, s87
	s_and_b32 s87, s2, 0xffffff80
	s_or_b32 s2, s86, s87
	v_lshl_or_b32 v64, s2, 2, v48
	v_min_i32_e32 v48, 0x61a7, v64
	v_lshl_or_b32 v54, v48, 5, v66
	v_ashrrev_i32_e32 v55, 31, v54
	v_lshl_add_u64 v[56:57], v[54:55], 4, s[8:9]
	v_max_i32_e32 v48, 1, v54
	v_mov_b32_e32 v49, 0
	v_lshl_add_u64 v[58:59], v[48:49], 4, s[8:9]
	global_load_dwordx4 v[48:51], v[56:57], off
	global_load_dword v80, v[56:57], off offset:24
	global_load_dword v55, v[58:59], off offset:-8
	s_load_dword s10, s[0:1], 0x48
	s_waitcnt vmcnt(13)
	ds_write_b128 v46, v[14:17] offset:12800
	s_waitcnt vmcnt(12)
	ds_write_b128 v46, v[22:25] offset:16896
	s_waitcnt vmcnt(10)
	ds_write_b128 v46, v[42:45] offset:20992
	s_waitcnt vmcnt(9)
	v_cvt_f16_f32_e32 v14, v34
	v_cvt_f16_f32_e32 v15, v37
	v_cvt_pk_f16_f32 v17, v35, v36
	s_waitcnt vmcnt(8)
	v_cvt_f16_f32_e32 v23, v41
	v_pack_b32_f16 v16, v14, v17
	v_alignbit_b32 v17, v15, v17, 16
	v_cvt_f16_f32_e32 v15, v38
	v_cvt_pk_f16_f32 v24, v39, v40
	v_lshlrev_b32_e32 v14, 3, v0
	v_alignbit_b32 v23, v23, v24, 16
	v_pack_b32_f16 v22, v15, v24
	s_waitcnt vmcnt(7)
	v_cvt_f16_f32_e32 v15, v18
	ds_write2st64_b64 v14, v[16:17], v[22:23] offset1:4
	v_cvt_pk_f16_f32 v17, v19, v20
	v_cvt_f16_f32_e32 v18, v21
	v_pack_b32_f16 v16, v15, v17
	s_waitcnt vmcnt(6)
	v_cvt_f16_f32_e32 v15, v26
	v_cvt_f16_f32_e32 v19, v29
	s_waitcnt vmcnt(5)
	v_cvt_f16_f32_e32 v6, v6
	v_cvt_pk_f16_f32 v7, v7, v8
	v_cvt_f16_f32_e32 v8, v9
	s_waitcnt vmcnt(4)
	v_cvt_f16_f32_e32 v9, v10
	v_cvt_f16_f32_e32 v10, v13
	v_cvt_pk_f16_f32 v20, v27, v28
	v_cvt_pk_f16_f32 v11, v11, v12
	v_alignbit_b32 v17, v18, v17, 16
	v_pack_b32_f16 v18, v15, v20
	v_alignbit_b32 v19, v19, v20, 16
	v_pack_b32_f16 v6, v6, v7
	v_alignbit_b32 v7, v8, v7, 16
	v_pack_b32_f16 v8, v9, v11
	v_alignbit_b32 v9, v10, v11, 16
	ds_write_b128 v46, v[30:33] offset:25088
	ds_write2st64_b64 v14, v[16:17], v[18:19] offset0:8 offset1:12
	ds_write2st64_b64 v14, v[6:7], v[8:9] offset0:16 offset1:20
	s_and_saveexec_b64 s[2:3], vcc
	s_cbranch_execnz .LBB4_74
	s_or_b64 exec, exec, s[2:3]
	s_and_saveexec_b64 s[2:3], vcc
	s_cbranch_execnz .LBB4_75
